# epilogue un-stagger barrier moved behind the bias loads / first convert group; attention prologue: ip-sum reduce waits only for its own load
# speedup vs baseline: 1.0089x; 1.0029x over previous
_Z11attn_kernelPKDF16_PDF16_PKf:
	s_load_dwordx2 s[4:5], s[0:1], 0x10
	s_load_dwordx2 s[6:7], s[0:1], 0x0
	v_and_b32_e32 v10, 63, v0
	v_lshlrev_b32_e32 v1, 2, v10
	s_ashr_i32 s8, s2, 5
	s_waitcnt lgkmcnt(0)
	global_load_dword v11, v1, s[4:5]
	s_lshl_b32 s3, s2, 5
	s_ashr_i32 s9, s8, 31
	s_and_b32 s3, s3, 0x300
	s_mul_hi_i32 s11, s8, 0x780000
	s_mul_i32 s12, s8, 0x780000
	s_lshl_b64 s[8:9], s[8:9], 10
	s_or_b32 s8, s8, s3
	s_mul_i32 s13, s9, 0x1e00
	s_mul_hi_u32 s14, s8, 0x1e00
	s_and_b32 s10, s2, 7
	s_mul_i32 s15, s8, 0x1e00
	s_add_i32 s14, s14, s13
	s_add_u32 s15, s6, s15
	s_addc_u32 s14, s7, s14
	s_mulk_i32 s10, 0xa0
	s_add_u32 s12, s6, s12
	s_addc_u32 s11, s7, s11
	s_lshl_b32 s16, s10, 1
	s_add_u32 s10, s12, s16
	s_addc_u32 s11, s11, 0
	v_readfirstlane_b32 s22, v0
	s_add_u32 s12, s10, 0xa00
	v_and_b32_e32 v4, 31, v0
	s_addc_u32 s13, s11, 0
	s_lshr_b32 s18, s22, 6
	s_movk_i32 s5, 0xf00
	s_add_u32 s10, s15, s16
	v_lshl_or_b32 v1, s18, 5, v4
	v_mov_b32_e32 v201, 0
	v_bfe_u32 v5, v0, 5, 1
	s_addc_u32 s11, s14, 0
	v_mad_u64_u32 v[34:35], s[14:15], v1, s5, 0
	v_mov_b32_e32 v3, v201
	v_lshlrev_b32_e32 v2, 4, v5
	s_mul_i32 s19, s18, 0xa0
	v_lshl_add_u64 v[8:9], v[34:35], 1, s[10:11]
	s_mov_b32 s17, 0xcccccccd
	v_add_u32_e32 v7, s19, v10
	v_lshl_add_u64 v[8:9], v[8:9], 0, v[2:3]
	v_mul_hi_u32 v12, v7, s17
	v_add_u32_e32 v6, 64, v7
	global_load_dwordx4 v[144:147], v[8:9], off
	global_load_dwordx4 v[148:151], v[8:9], off offset:32
	global_load_dwordx4 v[152:155], v[8:9], off offset:64
	global_load_dwordx4 v[156:159], v[8:9], off offset:96
	global_load_dwordx4 v[160:163], v[8:9], off offset:128
	global_load_dwordx4 v[164:167], v[8:9], off offset:160
	global_load_dwordx4 v[168:171], v[8:9], off offset:192
	global_load_dwordx4 v[172:175], v[8:9], off offset:224
	v_lshrrev_b32_e32 v3, 4, v12
	v_mul_hi_u32 v13, v6, s17
	v_mul_lo_u32 v14, v3, 20
	v_lshrrev_b32_e32 v15, 4, v13
	s_mulk_i32 s18, 0xa00
	s_movk_i32 s4, 0x1e00
	v_lshrrev_b32_e32 v12, 6, v12
	v_sub_u32_e32 v14, v7, v14
	v_mul_lo_u32 v16, v15, 20
	s_add_i32 s23, s18, 0
	v_mul_lo_u32 v3, v3, s4
	v_lshrrev_b32_e32 v13, 6, v13
	v_bitop3_b32 v12, v12, v14, 3 bitop3:0x6c
	v_sub_u32_e32 v14, v6, v16
	s_add_i32 s24, s23, 0x5000
	v_lshl_or_b32 v200, v12, 4, v3
	v_bitop3_b32 v3, v13, v14, 3 bitop3:0x6c
	global_load_dwordx4 v[176:179], v[8:9], off offset:256
	global_load_dwordx4 v[180:183], v[8:9], off offset:288
	v_mul_lo_u32 v8, v15, s4
	s_mov_b64 s[10:11], s[12:13]
	s_mov_b32 m0, s24
	s_add_i32 s25, s23, 0x5400
	v_lshl_or_b32 v202, v3, 4, v8
	v_mbcnt_lo_u32_b32 v3, -1, 0
	global_load_lds_dwordx4 v200, s[10:11]
	s_mov_b32 m0, s25
	v_mbcnt_hi_u32_b32 v3, -1, v3
	global_load_lds_dwordx4 v202, s[10:11]
	v_and_b32_e32 v8, 64, v3
	v_xor_b32_e32 v9, 32, v3
	v_add_u32_e32 v8, 64, v8
	v_cmp_lt_i32_e32 vcc, v9, v8
	v_xor_b32_e32 v12, 16, v3
	v_xor_b32_e32 v13, 8, v3
	v_cndmask_b32_e32 v9, v3, v9, vcc
	v_lshlrev_b32_e32 v9, 2, v9
	s_waitcnt vmcnt(12)
	ds_bpermute_b32 v9, v9, v11
	v_cmp_lt_i32_e32 vcc, v12, v8
	v_xor_b32_e32 v14, 4, v3
	v_xor_b32_e32 v15, 2, v3
	v_cndmask_b32_e32 v12, v3, v12, vcc
	v_lshlrev_b32_e32 v12, 2, v12
	s_waitcnt lgkmcnt(0)
	v_add_f32_e32 v9, v11, v9
	ds_bpermute_b32 v11, v12, v9
	v_cmp_lt_i32_e32 vcc, v13, v8
	v_xor_b32_e32 v12, 1, v3
	s_waitcnt lgkmcnt(0)
	v_add_f32_e32 v9, v9, v11
	v_cndmask_b32_e32 v13, v3, v13, vcc
	v_lshlrev_b32_e32 v13, 2, v13
	ds_bpermute_b32 v11, v13, v9
	v_cmp_lt_i32_e32 vcc, v14, v8
	s_waitcnt lgkmcnt(0)
	v_add_f32_e32 v9, v9, v11
	v_cndmask_b32_e32 v13, v3, v14, vcc
	v_lshlrev_b32_e32 v13, 2, v13
	ds_bpermute_b32 v11, v13, v9
	v_cmp_lt_i32_e32 vcc, v15, v8
	s_waitcnt lgkmcnt(0)
	v_add_f32_e32 v9, v9, v11
	v_cndmask_b32_e32 v14, v3, v15, vcc
	v_cmp_lt_i32_e32 vcc, v12, v8
	s_nop 1
	v_cndmask_b32_e32 v8, v3, v12, vcc
	v_lshlrev_b32_e32 v12, 2, v14
	ds_bpermute_b32 v11, v12, v9
	v_add_u32_e32 v3, 0x80, v7
	v_mul_hi_u32 v13, v3, s17
	v_lshlrev_b32_e32 v8, 2, v8
	v_lshrrev_b32_e32 v12, 4, v13
	s_waitcnt lgkmcnt(0)
	v_add_f32_e32 v39, v9, v11
	ds_bpermute_b32 v40, v8, v39
	v_mul_lo_u32 v14, v12, 20
	v_lshrrev_b32_e32 v13, 6, v13
	v_sub_u32_e32 v14, v3, v14
	v_bitop3_b32 v9, v13, v14, 3 bitop3:0x6c
	v_mul_lo_u32 v8, v12, s4
	v_lshl_or_b32 v204, v9, 4, v8
	v_cmp_lt_u32_e32 vcc, 31, v10
	v_cmp_gt_u32_e64 s[4:5], 32, v10
	s_and_saveexec_b64 s[14:15], s[4:5]
	s_cbranch_execz .LBB1_2
	s_add_i32 m0, s23, 0x5800
	s_nop 0
	global_load_lds_dwordx4 v204, s[10:11]

.LBB2_8:
	s_cmp_lt_i32 s61, 5
	s_cselect_b64 vcc, -1, 0
	v_lshl_or_b32 v142, s61, 8, v144
	v_cndmask_b32_e32 v140, 1.0, v148, vcc
	v_lshl_add_u32 v149, s62, 8, v1
	v_ashrrev_i32_e32 v143, 31, v142
	v_lshl_add_u64 v[142:143], v[142:143], 1, s[20:21]
	v_mad_i64_i32 v[150:151], s[26:27], v149, s56, 0
	v_pk_mul_f32 v[128:129], v[140:141], v[128:129] op_sel_hi:[0,1]
	v_pk_mul_f32 v[126:127], v[140:141], v[126:127] op_sel_hi:[0,1]
	v_pk_mul_f32 v[152:153], v[140:141], v[124:125] op_sel_hi:[0,1]
	v_pk_mul_f32 v[124:125], v[140:141], v[122:123] op_sel_hi:[0,1]
	v_lshl_add_u64 v[150:151], v[150:151], 1, v[142:143]
	v_cvt_pk_f16_f32 v122, v126, v127
	v_cvt_pk_f16_f32 v123, v128, v129
	v_cvt_pk_f16_f32 v124, v124, v125
	v_cvt_pk_f16_f32 v125, v152, v153
	s_cmpk_gt_u32 s3, 0xff
	s_cbranch_scc1 .Lus_g0_a
	s_barrier
.Lus_g0_a:
	global_store_dwordx4 v[150:151], v[122:125], off
	v_pk_mul_f32 v[120:121], v[140:141], v[120:121] op_sel_hi:[0,1]
	v_pk_mul_f32 v[118:119], v[140:141], v[118:119] op_sel_hi:[0,1]
	v_pk_mul_f32 v[122:123], v[140:141], v[116:117] op_sel_hi:[0,1]
	v_pk_mul_f32 v[116:117], v[140:141], v[114:115] op_sel_hi:[0,1]
	v_cvt_pk_f16_f32 v114, v118, v119
	v_cvt_pk_f16_f32 v115, v120, v121
	v_cvt_pk_f16_f32 v116, v116, v117
	v_cvt_pk_f16_f32 v117, v122, v123
	global_store_dwordx4 v[150:151], v[114:117], off offset:256
	v_pk_mul_f32 v[112:113], v[140:141], v[112:113] op_sel_hi:[0,1]
	v_pk_mul_f32 v[110:111], v[140:141], v[110:111] op_sel_hi:[0,1]
	v_or_b32_e32 v114, 16, v149
	v_mad_i64_i32 v[114:115], s[26:27], v114, s56, 0
	v_pk_mul_f32 v[116:117], v[140:141], v[108:109] op_sel_hi:[0,1]
	v_pk_mul_f32 v[108:109], v[140:141], v[106:107] op_sel_hi:[0,1]
	v_lshl_add_u64 v[114:115], v[114:115], 1, v[142:143]
	v_cvt_pk_f16_f32 v106, v110, v111
	v_cvt_pk_f16_f32 v107, v112, v113
	v_cvt_pk_f16_f32 v108, v108, v109
	v_cvt_pk_f16_f32 v109, v116, v117
	global_store_dwordx4 v[114:115], v[106:109], off
	v_pk_mul_f32 v[104:105], v[140:141], v[104:105] op_sel_hi:[0,1]
	v_pk_mul_f32 v[102:103], v[140:141], v[102:103] op_sel_hi:[0,1]
	v_pk_mul_f32 v[106:107], v[140:141], v[100:101] op_sel_hi:[0,1]
	v_pk_mul_f32 v[100:101], v[140:141], v[98:99] op_sel_hi:[0,1]
	v_cvt_pk_f16_f32 v98, v102, v103
	v_cvt_pk_f16_f32 v99, v104, v105
	v_cvt_pk_f16_f32 v100, v100, v101
	v_cvt_pk_f16_f32 v101, v106, v107
	global_store_dwordx4 v[114:115], v[98:101], off offset:256
	v_pk_mul_f32 v[96:97], v[140:141], v[96:97] op_sel_hi:[0,1]
	v_pk_mul_f32 v[94:95], v[140:141], v[94:95] op_sel_hi:[0,1]
	v_or_b32_e32 v98, 32, v149
	v_mad_i64_i32 v[98:99], s[26:27], v98, s56, 0
	v_pk_mul_f32 v[100:101], v[140:141], v[92:93] op_sel_hi:[0,1]
	v_pk_mul_f32 v[92:93], v[140:141], v[90:91] op_sel_hi:[0,1]
	v_lshl_add_u64 v[98:99], v[98:99], 1, v[142:143]
	v_cvt_pk_f16_f32 v90, v94, v95
	v_cvt_pk_f16_f32 v91, v96, v97
	v_cvt_pk_f16_f32 v92, v92, v93
	v_cvt_pk_f16_f32 v93, v100, v101
	global_store_dwordx4 v[98:99], v[90:93], off
	v_pk_mul_f32 v[88:89], v[140:141], v[88:89] op_sel_hi:[0,1]
	v_pk_mul_f32 v[86:87], v[140:141], v[86:87] op_sel_hi:[0,1]
	v_pk_mul_f32 v[90:91], v[140:141], v[84:85] op_sel_hi:[0,1]
	v_pk_mul_f32 v[84:85], v[140:141], v[82:83] op_sel_hi:[0,1]
	v_cvt_pk_f16_f32 v82, v86, v87
	v_cvt_pk_f16_f32 v83, v88, v89
	v_cvt_pk_f16_f32 v84, v84, v85
	v_cvt_pk_f16_f32 v85, v90, v91
	global_store_dwordx4 v[98:99], v[82:85], off offset:256
	v_pk_mul_f32 v[80:81], v[140:141], v[80:81] op_sel_hi:[0,1]
	v_pk_mul_f32 v[78:79], v[140:141], v[78:79] op_sel_hi:[0,1]
	v_or_b32_e32 v82, 48, v149
	v_mad_i64_i32 v[82:83], s[26:27], v82, s56, 0
	v_pk_mul_f32 v[84:85], v[140:141], v[76:77] op_sel_hi:[0,1]
	v_pk_mul_f32 v[76:77], v[140:141], v[74:75] op_sel_hi:[0,1]
	v_lshl_add_u64 v[82:83], v[82:83], 1, v[142:143]
	v_cvt_pk_f16_f32 v74, v78, v79
	v_cvt_pk_f16_f32 v75, v80, v81
	v_cvt_pk_f16_f32 v76, v76, v77
	v_cvt_pk_f16_f32 v77, v84, v85
	global_store_dwordx4 v[82:83], v[74:77], off
	v_pk_mul_f32 v[72:73], v[140:141], v[72:73] op_sel_hi:[0,1]
	v_pk_mul_f32 v[70:71], v[140:141], v[70:71] op_sel_hi:[0,1]
	v_pk_mul_f32 v[74:75], v[140:141], v[68:69] op_sel_hi:[0,1]
	v_pk_mul_f32 v[68:69], v[140:141], v[66:67] op_sel_hi:[0,1]
	v_cvt_pk_f16_f32 v66, v70, v71
	v_cvt_pk_f16_f32 v67, v72, v73
	v_cvt_pk_f16_f32 v68, v68, v69
	v_cvt_pk_f16_f32 v69, v74, v75
	global_store_dwordx4 v[82:83], v[66:69], off offset:256
	v_pk_mul_f32 v[64:65], v[140:141], v[64:65] op_sel_hi:[0,1]
	v_pk_mul_f32 v[62:63], v[140:141], v[62:63] op_sel_hi:[0,1]
	v_add_u32_e32 v66, 0x80, v149
	v_mad_i64_i32 v[66:67], s[26:27], v66, s56, 0
	v_pk_mul_f32 v[68:69], v[140:141], v[60:61] op_sel_hi:[0,1]
	v_pk_mul_f32 v[60:61], v[140:141], v[58:59] op_sel_hi:[0,1]
	v_lshl_add_u64 v[66:67], v[66:67], 1, v[142:143]
	v_cvt_pk_f16_f32 v58, v62, v63
	v_cvt_pk_f16_f32 v59, v64, v65
	v_cvt_pk_f16_f32 v60, v60, v61
	v_cvt_pk_f16_f32 v61, v68, v69
	global_store_dwordx4 v[66:67], v[58:61], off
	v_pk_mul_f32 v[56:57], v[140:141], v[56:57] op_sel_hi:[0,1]
	v_pk_mul_f32 v[54:55], v[140:141], v[54:55] op_sel_hi:[0,1]
	v_pk_mul_f32 v[58:59], v[140:141], v[52:53] op_sel_hi:[0,1]
	v_pk_mul_f32 v[52:53], v[140:141], v[50:51] op_sel_hi:[0,1]
	v_cvt_pk_f16_f32 v50, v54, v55
	v_cvt_pk_f16_f32 v51, v56, v57
	v_cvt_pk_f16_f32 v52, v52, v53
	v_cvt_pk_f16_f32 v53, v58, v59
	global_store_dwordx4 v[66:67], v[50:53], off offset:256
	v_pk_mul_f32 v[48:49], v[140:141], v[48:49] op_sel_hi:[0,1]
	v_pk_mul_f32 v[46:47], v[140:141], v[46:47] op_sel_hi:[0,1]
	v_add_u32_e32 v50, 0x90, v149
	v_mad_i64_i32 v[50:51], s[26:27], v50, s56, 0
	v_pk_mul_f32 v[52:53], v[140:141], v[44:45] op_sel_hi:[0,1]
	v_pk_mul_f32 v[44:45], v[140:141], v[42:43] op_sel_hi:[0,1]
	v_lshl_add_u64 v[50:51], v[50:51], 1, v[142:143]
	v_cvt_pk_f16_f32 v42, v46, v47
	v_cvt_pk_f16_f32 v43, v48, v49
	v_cvt_pk_f16_f32 v44, v44, v45
	v_cvt_pk_f16_f32 v45, v52, v53
	global_store_dwordx4 v[50:51], v[42:45], off
	v_pk_mul_f32 v[40:41], v[140:141], v[40:41] op_sel_hi:[0,1]
	v_pk_mul_f32 v[38:39], v[140:141], v[38:39] op_sel_hi:[0,1]
	v_pk_mul_f32 v[42:43], v[140:141], v[36:37] op_sel_hi:[0,1]
	v_pk_mul_f32 v[36:37], v[140:141], v[34:35] op_sel_hi:[0,1]
	v_cvt_pk_f16_f32 v34, v38, v39
	v_cvt_pk_f16_f32 v35, v40, v41
	v_cvt_pk_f16_f32 v36, v36, v37
	v_cvt_pk_f16_f32 v37, v42, v43
	global_store_dwordx4 v[50:51], v[34:37], off offset:256
	v_pk_mul_f32 v[32:33], v[140:141], v[32:33] op_sel_hi:[0,1]
	v_pk_mul_f32 v[30:31], v[140:141], v[30:31] op_sel_hi:[0,1]
	v_add_u32_e32 v34, 0xa0, v149
	v_mad_i64_i32 v[34:35], s[26:27], v34, s56, 0
	v_pk_mul_f32 v[36:37], v[140:141], v[28:29] op_sel_hi:[0,1]
	v_pk_mul_f32 v[28:29], v[140:141], v[26:27] op_sel_hi:[0,1]
	v_lshl_add_u64 v[34:35], v[34:35], 1, v[142:143]
	v_cvt_pk_f16_f32 v26, v30, v31
	v_cvt_pk_f16_f32 v27, v32, v33
	v_cvt_pk_f16_f32 v28, v28, v29
	v_cvt_pk_f16_f32 v29, v36, v37
	global_store_dwordx4 v[34:35], v[26:29], off
	v_pk_mul_f32 v[24:25], v[140:141], v[24:25] op_sel_hi:[0,1]
	v_pk_mul_f32 v[22:23], v[140:141], v[22:23] op_sel_hi:[0,1]
	v_pk_mul_f32 v[26:27], v[140:141], v[20:21] op_sel_hi:[0,1]
	v_pk_mul_f32 v[20:21], v[140:141], v[18:19] op_sel_hi:[0,1]
	v_cvt_pk_f16_f32 v18, v22, v23
	v_cvt_pk_f16_f32 v19, v24, v25
	v_cvt_pk_f16_f32 v20, v20, v21
	v_cvt_pk_f16_f32 v21, v26, v27
	global_store_dwordx4 v[34:35], v[18:21], off offset:256
	v_pk_mul_f32 v[16:17], v[140:141], v[16:17] op_sel_hi:[0,1]
	v_pk_mul_f32 v[14:15], v[140:141], v[14:15] op_sel_hi:[0,1]
	v_add_u32_e32 v18, 0xb0, v149
	v_mad_i64_i32 v[18:19], s[26:27], v18, s56, 0
	v_pk_mul_f32 v[20:21], v[140:141], v[12:13] op_sel_hi:[0,1]
	v_pk_mul_f32 v[12:13], v[140:141], v[10:11] op_sel_hi:[0,1]
	v_lshl_add_u64 v[18:19], v[18:19], 1, v[142:143]
	v_cvt_pk_f16_f32 v10, v14, v15
	v_cvt_pk_f16_f32 v11, v16, v17
	v_cvt_pk_f16_f32 v12, v12, v13
	v_cvt_pk_f16_f32 v13, v20, v21
	global_store_dwordx4 v[18:19], v[10:13], off
	v_pk_mul_f32 v[8:9], v[140:141], v[8:9] op_sel_hi:[0,1]
	v_pk_mul_f32 v[6:7], v[140:141], v[6:7] op_sel_hi:[0,1]
	v_pk_mul_f32 v[10:11], v[140:141], v[4:5] op_sel_hi:[0,1]
	v_pk_mul_f32 v[4:5], v[140:141], v[2:3] op_sel_hi:[0,1]
	v_cvt_pk_f16_f32 v2, v6, v7
	v_cvt_pk_f16_f32 v3, v8, v9
	v_cvt_pk_f16_f32 v4, v4, v5
	v_cvt_pk_f16_f32 v5, v10, v11
	s_and_b64 vcc, exec, s[8:9]
	s_mov_b32 s62, s60
	s_mov_b32 s61, s59
	s_mov_b64 s[26:27], s[6:7]
	s_mov_b64 s[28:29], s[4:5]
	global_store_dwordx4 v[18:19], v[2:5], off offset:256
	s_cmpk_gt_u32 s3, 0xff
	s_cbranch_scc0 .Lus_g0_b
	s_barrier

.LBB3_10:
	v_lshl_or_b32 v128, s68, 8, v168
	v_ashrrev_i32_e32 v129, 31, v128
	v_lshlrev_b64 v[154:155], 2, v[128:129]
	v_lshl_add_u64 v[128:129], s[10:11], 0, v[154:155]
	global_load_dwordx4 v[140:143], v[128:129], off
	global_load_dwordx4 v[136:139], v[128:129], off offset:64
	global_load_dwordx4 v[132:135], v[128:129], off offset:512
	s_nop 0
	global_load_dwordx4 v[128:131], v[128:129], off offset:576
	v_lshl_add_u32 v180, s67, 8, v167
	v_add_u32_e32 v178, 0x80, v180
	v_mad_i64_i32 v[156:157], s[30:31], v180, s42, 0
	v_or_b32_e32 v172, 16, v180
	v_or_b32_e32 v174, 32, v180
	v_or_b32_e32 v176, 48, v180
	v_mad_i64_i32 v[178:179], s[30:31], v178, s42, 0
	v_lshl_add_u64 v[154:155], s[8:9], 0, v[154:155]
	v_mad_i64_i32 v[172:173], s[30:31], v172, s42, 0
	v_mad_i64_i32 v[174:175], s[30:31], v174, s42, 0
	v_mad_i64_i32 v[176:177], s[30:31], v176, s42, 0
	v_lshl_add_u64 v[156:157], v[156:157], 2, v[154:155]
	v_lshl_add_u64 v[178:179], v[178:179], 2, v[154:155]
	v_lshl_add_u64 v[172:173], v[172:173], 2, v[154:155]
	v_lshl_add_u64 v[174:175], v[174:175], 2, v[154:155]
	v_lshl_add_u64 v[176:177], v[176:177], 2, v[154:155]
	s_mov_b32 s67, s66
	s_mov_b32 s68, s65
	s_mov_b64 s[34:35], s[28:29]
	s_cmpk_gt_u32 s41, 0xff
	s_cbranch_scc1 .Lus_g1_a
	s_barrier
.Lus_g1_a:
	s_mov_b64 vcc, s[0:1]
	s_waitcnt vmcnt(0)
	v_pk_add_f32 v[118:119], v[142:143], v[118:119]
	v_pk_add_f32 v[116:117], v[140:141], v[116:117]
	v_pk_add_f32 v[126:127], v[138:139], v[126:127]
	v_pk_add_f32 v[50:51], v[130:131], v[50:51]
	v_pk_add_f32 v[48:49], v[128:129], v[48:49]
	v_pk_add_f32 v[124:125], v[136:137], v[124:125]
	v_pk_add_f32 v[122:123], v[134:135], v[122:123]
	v_pk_add_f32 v[120:121], v[132:133], v[120:121]
	v_pk_add_f32 v[114:115], v[130:131], v[114:115]
	v_pk_add_f32 v[112:113], v[128:129], v[112:113]
	v_pk_add_f32 v[110:111], v[142:143], v[110:111]
	v_pk_add_f32 v[108:109], v[140:141], v[108:109]
	v_pk_add_f32 v[106:107], v[138:139], v[106:107]
	v_pk_add_f32 v[104:105], v[136:137], v[104:105]
	v_pk_add_f32 v[102:103], v[134:135], v[102:103]
	v_pk_add_f32 v[100:101], v[132:133], v[100:101]
	v_pk_add_f32 v[98:99], v[130:131], v[98:99]
	v_pk_add_f32 v[96:97], v[128:129], v[96:97]
	v_pk_add_f32 v[94:95], v[142:143], v[94:95]
	v_pk_add_f32 v[92:93], v[140:141], v[92:93]
	v_pk_add_f32 v[90:91], v[138:139], v[90:91]
	v_pk_add_f32 v[88:89], v[136:137], v[88:89]
	v_pk_add_f32 v[86:87], v[134:135], v[86:87]
	v_pk_add_f32 v[84:85], v[132:133], v[84:85]
	v_pk_add_f32 v[82:83], v[130:131], v[82:83]
	v_pk_add_f32 v[80:81], v[128:129], v[80:81]
	v_pk_add_f32 v[78:79], v[142:143], v[78:79]
	v_pk_add_f32 v[76:77], v[140:141], v[76:77]
	v_pk_add_f32 v[74:75], v[138:139], v[74:75]
	v_pk_add_f32 v[72:73], v[136:137], v[72:73]
	v_pk_add_f32 v[70:71], v[134:135], v[70:71]
	v_pk_add_f32 v[68:69], v[132:133], v[68:69]
	v_pk_add_f32 v[66:67], v[130:131], v[66:67]
	v_pk_add_f32 v[64:65], v[128:129], v[64:65]
	v_pk_add_f32 v[62:63], v[142:143], v[62:63]
	v_pk_add_f32 v[60:61], v[140:141], v[60:61]
	v_pk_add_f32 v[58:59], v[138:139], v[58:59]
	v_pk_add_f32 v[56:57], v[136:137], v[56:57]
	v_pk_add_f32 v[54:55], v[134:135], v[54:55]
	v_pk_add_f32 v[52:53], v[132:133], v[52:53]
	global_store_dwordx4 v[156:157], v[116:119], off
	global_store_dwordx4 v[156:157], v[124:127], off offset:64
	global_store_dwordx4 v[156:157], v[120:123], off offset:512
	global_store_dwordx4 v[156:157], v[112:115], off offset:576
	global_store_dwordx4 v[172:173], v[108:111], off
	global_store_dwordx4 v[172:173], v[104:107], off offset:64
	global_store_dwordx4 v[172:173], v[100:103], off offset:512
	global_store_dwordx4 v[172:173], v[96:99], off offset:576
	global_store_dwordx4 v[174:175], v[92:95], off
	global_store_dwordx4 v[174:175], v[88:91], off offset:64
	global_store_dwordx4 v[174:175], v[84:87], off offset:512
	global_store_dwordx4 v[174:175], v[80:83], off offset:576
	global_store_dwordx4 v[176:177], v[76:79], off
	global_store_dwordx4 v[176:177], v[72:75], off offset:64
	global_store_dwordx4 v[176:177], v[68:71], off offset:512
	global_store_dwordx4 v[176:177], v[64:67], off offset:576
	global_store_dwordx4 v[178:179], v[60:63], off
	global_store_dwordx4 v[178:179], v[56:59], off offset:64
	global_store_dwordx4 v[178:179], v[52:55], off offset:512
	global_store_dwordx4 v[178:179], v[48:51], off offset:576
	v_pk_add_f32 v[34:35], v[130:131], v[34:35]
	v_pk_add_f32 v[32:33], v[128:129], v[32:33]
	v_add_u32_e32 v48, 0x90, v180
	v_mad_i64_i32 v[48:49], s[30:31], v48, s42, 0
	v_lshl_add_u64 v[48:49], v[48:49], 2, v[154:155]
	global_store_dwordx4 v[48:49], v[32:35], off offset:576
	v_pk_add_f32 v[46:47], v[142:143], v[46:47]
	v_pk_add_f32 v[44:45], v[140:141], v[44:45]
	v_add_u32_e32 v32, 0xa0, v180
	v_mad_i64_i32 v[32:33], s[30:31], v32, s42, 0
	v_pk_add_f32 v[42:43], v[138:139], v[42:43]
	v_pk_add_f32 v[40:41], v[136:137], v[40:41]
	v_pk_add_f32 v[38:39], v[134:135], v[38:39]
	v_pk_add_f32 v[36:37], v[132:133], v[36:37]
	v_lshl_add_u64 v[32:33], v[32:33], 2, v[154:155]
	v_pk_add_f32 v[18:19], v[130:131], v[18:19]
	v_pk_add_f32 v[16:17], v[128:129], v[16:17]
	global_store_dwordx4 v[48:49], v[44:47], off
	global_store_dwordx4 v[48:49], v[40:43], off offset:64
	global_store_dwordx4 v[48:49], v[36:39], off offset:512
	global_store_dwordx4 v[32:33], v[16:19], off offset:576
	v_pk_add_f32 v[30:31], v[142:143], v[30:31]
	v_pk_add_f32 v[28:29], v[140:141], v[28:29]
	v_add_u32_e32 v16, 0xb0, v180
	v_mad_i64_i32 v[16:17], s[30:31], v16, s42, 0
	v_pk_add_f32 v[26:27], v[138:139], v[26:27]
	v_pk_add_f32 v[24:25], v[136:137], v[24:25]
	v_pk_add_f32 v[22:23], v[134:135], v[22:23]
	v_pk_add_f32 v[20:21], v[132:133], v[20:21]
	v_lshl_add_u64 v[16:17], v[16:17], 2, v[154:155]
	v_pk_add_f32 v[14:15], v[142:143], v[14:15]
	v_pk_add_f32 v[12:13], v[140:141], v[12:13]
	v_pk_add_f32 v[10:11], v[138:139], v[10:11]
	v_pk_add_f32 v[8:9], v[136:137], v[8:9]
	v_pk_add_f32 v[6:7], v[134:135], v[6:7]
	v_pk_add_f32 v[4:5], v[132:133], v[4:5]
	v_pk_add_f32 v[2:3], v[130:131], v[2:3]
	v_pk_add_f32 v[0:1], v[128:129], v[0:1]
	s_mov_b64 s[30:31], s[4:5]
	global_store_dwordx4 v[32:33], v[28:31], off
	global_store_dwordx4 v[32:33], v[24:27], off offset:64
	global_store_dwordx4 v[32:33], v[20:23], off offset:512
	global_store_dwordx4 v[16:17], v[12:15], off
	global_store_dwordx4 v[16:17], v[8:11], off offset:64
	global_store_dwordx4 v[16:17], v[4:7], off offset:512
	global_store_dwordx4 v[16:17], v[0:3], off offset:576
	s_cmpk_gt_u32 s41, 0xff
	s_cbranch_scc0 .Lus_g1_b
	s_barrier
